# speedup vs baseline: 1.0656x; 1.0062x over previous
_Z11gemm_kernelILi4ELi2ELi2ELi4ELi4ELi3ELi2ELb0EEvPKDF16_iiS1_iiiiiPKfPfPDF16_i:
	s_and_b32 s3, s2, 7
	s_lshr_b32 s4, s2, 3
	s_lshr_b32 s5, s4, 2
	s_and_b32 s4, s4, 3
	s_lshl_b32 s5, s5, 2
	s_and_b32 s6, s3, 3
	s_add_u32 s5, s5, s6
	s_lshr_b32 s3, s3, 2
	s_lshl_b32 s3, s3, 2
	s_add_u32 s4, s4, s3
	s_and_b32 s6, s5, 7
	s_lshr_b32 s5, s5, 3
	s_lshl_b32 s5, s5, 3
	s_add_u32 s4, s4, s5
	s_lshl_b32 s4, s4, 3
	s_or_b32 s2, s4, s6
	s_load_dwordx4 s[8:11], s[0:1], 0x18
	s_load_dword s19, s[0:1], 0x28
	s_ashr_i32 s20, s2, 3
	s_and_b32 s5, s2, 7
	s_abs_i32 s2, s20
	s_waitcnt lgkmcnt(0)
	s_mul_i32 s3, s19, s10
	s_abs_i32 s4, s3
	v_cvt_f32_u32_e32 v1, s4
	s_sub_i32 s7, 0, s4
	s_xor_b32 s6, s20, s3
	s_ashr_i32 s6, s6, 31
	v_rcp_iflag_f32_e32 v1, v1
	s_nop 0
	v_mul_f32_e32 v1, 0x4f7ffffe, v1
	v_cvt_u32_f32_e32 v1, v1
	s_nop 0
	v_readfirstlane_b32 s12, v1
	s_mul_i32 s7, s7, s12
	s_mul_hi_u32 s7, s12, s7
	s_add_i32 s12, s12, s7
	s_mul_hi_u32 s7, s2, s12
	s_mul_i32 s12, s7, s4
	s_sub_i32 s2, s2, s12
	s_add_i32 s13, s7, 1
	s_sub_i32 s12, s2, s4
	s_cmp_ge_u32 s2, s4
	s_cselect_b32 s7, s13, s7
	s_cselect_b32 s2, s12, s2
	s_add_i32 s12, s7, 1
	s_cmp_ge_u32 s2, s4
	s_cselect_b32 s2, s12, s7
	s_xor_b32 s2, s2, s6
	s_sub_i32 s21, s2, s6
	s_lshl_b32 s2, s21, 3
	s_or_b32 s2, s2, s5
	s_cmp_ge_i32 s2, s11
	s_cbranch_scc1 .LBB5_85
	s_abs_i32 s11, s10
	v_cvt_f32_u32_e32 v1, s11
	s_mul_i32 s3, s21, s3
	s_sub_i32 s3, s20, s3
	s_xor_b32 s15, s3, s10
	v_rcp_iflag_f32_e32 v1, v1
	s_sub_i32 s14, 0, s11
	s_ashr_i32 s22, s15, 31
	s_abs_i32 s16, s3
	v_mul_f32_e32 v1, 0x4f7ffffe, v1
	v_cvt_u32_f32_e32 v1, v1
	s_load_dwordx4 s[4:7], s[0:1], 0x0
	s_load_dwordx2 s[12:13], s[0:1], 0x10
	v_lshrrev_b32_e32 v11, 2, v0
	v_lshrrev_b32_e32 v139, 6, v0
	v_readfirstlane_b32 s15, v1
	s_mul_i32 s14, s14, s15
	s_mul_hi_u32 s14, s15, s14
	s_add_i32 s15, s15, s14
	s_mul_hi_u32 s14, s16, s15
	s_mul_i32 s15, s14, s11
	s_sub_i32 s15, s16, s15
	s_add_i32 s17, s14, 1
	s_sub_i32 s16, s15, s11
	s_cmp_ge_u32 s15, s11
	s_cselect_b32 s14, s17, s14
	s_cselect_b32 s15, s16, s15
	s_add_i32 s16, s14, 1
	s_cmp_ge_u32 s15, s11
	s_cselect_b32 s11, s16, s14
	s_abs_i32 s14, s19
	v_cvt_f32_u32_e32 v1, s14
	s_xor_b32 s23, s11, s22
	s_sub_i32 s17, s23, s22
	s_mul_i32 s11, s17, s10
	v_rcp_iflag_f32_e32 v1, v1
	s_sub_i32 s3, s3, s11
	s_lshl_b32 s11, s3, 8
	s_lshl_b32 s16, s2, 8
	v_mul_f32_e32 v1, 0x4f7ffffe, v1
	v_cvt_u32_f32_e32 v1, v1
	s_xor_b32 s2, s9, s19
	s_abs_i32 s3, s9
	s_sub_i32 s9, 0, s14
	v_readfirstlane_b32 s15, v1
	s_mul_i32 s9, s9, s15
	s_mul_hi_u32 s9, s15, s9
	s_add_i32 s15, s15, s9
	s_mul_hi_u32 s9, s3, s15
	s_mul_i32 s15, s9, s14
	s_sub_i32 s3, s3, s15
	s_ashr_i32 s2, s2, 31
	s_add_i32 s15, s9, 1
	s_sub_i32 s18, s3, s14
	s_cmp_ge_u32 s3, s14
	s_cselect_b32 s9, s15, s9
	s_cselect_b32 s3, s18, s3
	s_add_i32 s15, s9, 1
	s_cmp_ge_u32 s3, s14
	s_cselect_b32 s3, s15, s9
	v_lshrrev_b32_e32 v1, 4, v0
	s_xor_b32 s3, s3, s2
	v_xor_b32_e32 v1, v1, v0
	s_sub_i32 s2, s3, s2
	v_lshlrev_b32_e32 v1, 3, v1
	s_mul_i32 s9, s2, s17
	v_or_b32_e32 v3, s16, v11
	s_waitcnt lgkmcnt(0)
	s_add_i32 s24, s7, -1
	v_and_b32_e32 v10, 24, v1
	v_add_u32_e32 v2, s9, v10
	v_min_i32_e32 v1, s24, v3
	s_ashr_i32 s18, s2, 5
	v_mad_u64_u32 v[8:9], s[2:3], v1, s6, v[2:3]
	v_or_b32_e32 v1, 0x80, v3
	v_min_i32_e32 v1, s24, v1
	v_mad_u64_u32 v[6:7], s[2:3], v1, s6, v[2:3]
	v_or_b32_e32 v1, s11, v11
	s_lshl_b32 s2, s8, 7
	v_mul_lo_u32 v1, v1, s8
	s_cmp_gt_i32 s18, 0
	v_add_u32_e32 v4, v2, v1
	v_add3_u32 v2, v1, s2, v2
	s_cselect_b64 s[14:15], -1, 0
	v_lshlrev_b32_e32 v143, 10, v139
	s_and_b64 vcc, exec, s[14:15]
	v_ashrrev_i32_e32 v9, 31, v8
	v_ashrrev_i32_e32 v7, 31, v6
	v_ashrrev_i32_e32 v5, 31, v4
	v_ashrrev_i32_e32 v3, 31, v2
	s_cbranch_vccz .LBB5_3
	v_readfirstlane_b32 s2, v143
	v_or_b32_e32 v1, 0x2000, v143
	v_lshl_add_u64 v[12:13], v[8:9], 1, s[4:5]
	s_mov_b32 m0, s2
	v_readfirstlane_b32 s2, v1
	v_or_b32_e32 v1, 0x4000, v143
	global_load_lds_dwordx4 v[12:13], off
	v_lshl_add_u64 v[12:13], v[6:7], 1, s[4:5]
	s_mov_b32 m0, s2
	v_readfirstlane_b32 s2, v1
	v_or_b32_e32 v1, 0x6000, v143
	global_load_lds_dwordx4 v[12:13], off
	v_lshl_add_u64 v[12:13], v[4:5], 1, s[12:13]
	s_mov_b32 m0, s2
	v_readfirstlane_b32 s2, v1
	global_load_lds_dwordx4 v[12:13], off
	v_lshl_add_u64 v[12:13], v[2:3], 1, s[12:13]
	s_mov_b32 m0, s2
	s_nop 0
	global_load_lds_dwordx4 v[12:13], off
